# speedup vs baseline: 1.0008x; 1.0008x over previous
_Z6k_pre2PKjPKiPiS3_PKfPKDv8_DF16_S5_S8_S2_PDF16_PhPf:
	s_mul_hi_i32 s21, s2, 0x55555556
	s_lshr_b32 s3, s21, 31
	s_add_i32 s21, s21, s3
	s_mul_i32 s3, s21, -3
	s_add_i32 s2, s3, s2
	s_cmp_lg_u32 s2, 0
	s_cbranch_scc0 .LBB1_9
	s_load_dwordx4 s[4:7], s[0:1], 0x28
	s_load_dwordx2 s[12:13], s[0:1], 0x38
	s_waitcnt lgkmcnt(0)
	v_lshlrev_b32_e32 v54, 4, v0
	global_load_dwordx4 v[56:59], v54, s[4:5]
	v_add_u32_e32 v55, 0x2000, v54
	global_load_dwordx4 v[60:63], v55, s[4:5]
	v_add_u32_e32 v55, 0x4000, v54
	global_load_dwordx4 v[64:67], v55, s[4:5]
	v_add_u32_e32 v55, 0x6000, v54
	global_load_dwordx4 v[68:71], v55, s[4:5]
	s_lshl_b32 s3, s21, 4
	s_lshl_b32 s2, s2, 3
	v_lshrrev_b32_e32 v1, 6, v0
	s_add_i32 s2, s2, s3
	v_or_b32_e32 v1, s2, v1
	v_add_u32_e32 v8, -8, v1
	v_and_b32_e32 v6, 3, v0
	s_movk_i32 s2, 0x186a
	v_bfe_u32 v1, v0, 2, 4
	v_lshlrev_b32_e32 v9, 3, v6
	v_mov_b32_e32 v3, 0
	v_cmp_gt_i32_e32 vcc, s2, v8
	s_and_saveexec_b64 s[2:3], vcc
	s_cbranch_execz .LBB1_3
	s_load_dwordx2 s[8:9], s[0:1], 0x20
	v_lshl_or_b32 v4, v8, 4, v1
	v_lshlrev_b32_e32 v2, 2, v9
	v_ashrrev_i32_e32 v5, 31, v4
	v_lshlrev_b64 v[4:5], 9, v[4:5]
	s_waitcnt lgkmcnt(0)
	v_lshl_add_u64 v[10:11], s[8:9], 0, v[2:3]
	v_lshl_add_u64 v[4:5], v[10:11], 0, v[4:5]
	global_load_dwordx4 v[10:13], v[4:5], off
	global_load_dwordx4 v[14:17], v[4:5], off offset:16
	global_load_dwordx4 v[30:33], v[4:5], off offset:128
	global_load_dwordx4 v[34:37], v[4:5], off offset:144
	global_load_dwordx4 v[38:41], v[4:5], off offset:256
	global_load_dwordx4 v[42:45], v[4:5], off offset:272
	global_load_dwordx4 v[46:49], v[4:5], off offset:384
	global_load_dwordx4 v[50:53], v[4:5], off offset:400
	s_waitcnt vmcnt(7)
	v_cvt_f16_f32_e32 v25, v10
	v_cvt_pk_f16_f32 v26, v11, v12
	s_waitcnt vmcnt(6)
	v_cvt_pk_f16_f32 v27, v13, v14
	v_cvt_pk_f16_f32 v28, v15, v16
	v_cvt_f16_f32_e32 v24, v17
	s_waitcnt vmcnt(5)
	v_cvt_f16_f32_e32 v20, v30
	v_cvt_pk_f16_f32 v23, v31, v32
	s_waitcnt vmcnt(4)
	v_cvt_pk_f16_f32 v22, v33, v34
	v_cvt_pk_f16_f32 v21, v35, v36
	v_cvt_f16_f32_e32 v19, v37
	s_waitcnt vmcnt(3)
	v_cvt_f16_f32_e32 v15, v38
	v_cvt_pk_f16_f32 v16, v39, v40
	s_waitcnt vmcnt(2)
	v_cvt_pk_f16_f32 v17, v41, v42
	v_cvt_pk_f16_f32 v18, v43, v44
	v_cvt_f16_f32_e32 v14, v45
	s_waitcnt vmcnt(1)
	v_cvt_f16_f32_e32 v13, v46
	s_waitcnt vmcnt(0)
	v_cvt_f16_f32_e32 v7, v53
	v_cvt_pk_f16_f32 v12, v47, v48
	v_cvt_pk_f16_f32 v11, v49, v50
	v_cvt_pk_f16_f32 v10, v51, v52
.LBB1_3:
	s_or_b64 exec, exec, s[2:3]
	s_load_dword s2, s[0:1], 0x6c
	s_load_dwordx2 s[14:15], s[0:1], 0x58
	s_load_dwordx4 s[8:11], s[0:1], 0x48
	v_lshlrev_b32_e32 v2, 4, v0
	v_and_b32_e32 v29, 63, v0
	s_waitcnt lgkmcnt(0)
	s_waitcnt vmcnt(0)
	ds_write_b128 v2, v[56:59]
	ds_write_b128 v2, v[60:63] offset:8192
	ds_write_b128 v2, v[64:67] offset:16384
	ds_write_b128 v2, v[68:71] offset:24576
	s_waitcnt lgkmcnt(0)
	s_barrier
	s_and_saveexec_b64 s[2:3], vcc
	s_cbranch_execz .LBB1_8
	v_lshlrev_b32_e32 v2, 2, v0
	v_lshrrev_b32_e32 v3, 4, v29
	v_lshlrev_b32_e32 v104, 4, v29
	v_and_or_b32 v2, v2, 60, v3
	s_mov_b32 s4, 0x5040100
	v_lshlrev_b32_e32 v105, 2, v2
	v_perm_b32 v2, v26, v25, s4
	v_alignbit_b32 v3, v27, v26, 16
	v_alignbit_b32 v4, v28, v27, 16
	v_alignbit_b32 v5, v24, v28, 16
	ds_read_b128 v[24:27], v104
	ds_bpermute_b32 v2, v105, v2
	ds_bpermute_b32 v3, v105, v3
	ds_bpermute_b32 v4, v105, v4
	ds_bpermute_b32 v5, v105, v5
	ds_read_b128 v[28:31], v104 offset:4096
	ds_read_b128 v[32:35], v104 offset:1024
	ds_read_b128 v[36:39], v104 offset:8192
	ds_read_b128 v[40:43], v104 offset:5120
	ds_read_b128 v[44:47], v104 offset:12288
	ds_read_b128 v[48:51], v104 offset:16384
	ds_read_b128 v[52:55], v104 offset:9216
	v_perm_b32 v20, v23, v20, s4
	v_alignbit_b32 v23, v22, v23, 16
	v_alignbit_b32 v22, v21, v22, 16
	v_alignbit_b32 v19, v19, v21, 16
	ds_read_b128 v[56:59], v104 offset:20480
	ds_read_b128 v[60:63], v104 offset:13312
	ds_read_b128 v[64:67], v104 offset:24576
	ds_read_b128 v[68:71], v104 offset:17408
	ds_bpermute_b32 v20, v105, v20
	ds_bpermute_b32 v21, v105, v23
	ds_bpermute_b32 v22, v105, v22
	ds_bpermute_b32 v23, v105, v19
	s_waitcnt lgkmcnt(14)
	v_mfma_f32_16x16x32_f16 v[24:27], v[24:27], v[2:5], 0
	ds_read_b128 v[72:75], v104 offset:28672
	ds_read_b128 v[76:79], v104 offset:21504
	ds_read_b128 v[80:83], v104 offset:25600
	ds_read_b128 v[84:87], v104 offset:29696
	v_mfma_f32_16x16x32_f16 v[28:31], v[28:31], v[2:5], 0
	v_lshlrev_b32_e32 v19, 1, v0
	v_and_b32_e32 v106, 0x60, v19
	v_perm_b32 v15, v16, v15, s4
	s_waitcnt lgkmcnt(14)
	v_mfma_f32_16x16x32_f16 v[36:39], v[36:39], v[2:5], 0
	v_alignbit_b32 v16, v17, v16, 16
	v_alignbit_b32 v17, v18, v17, 16
	v_alignbit_b32 v18, v14, v18, 16
	v_mfma_f32_16x16x32_f16 v[44:47], v[44:47], v[2:5], 0
	ds_bpermute_b32 v14, v105, v15
	ds_bpermute_b32 v15, v105, v16
	ds_bpermute_b32 v16, v105, v17
	s_waitcnt lgkmcnt(14)
	v_mfma_f32_16x16x32_f16 v[48:51], v[48:51], v[2:5], 0
	ds_bpermute_b32 v17, v105, v18
	v_perm_b32 v13, v12, v13, s4
	v_alignbit_b32 v12, v11, v12, 16
	s_waitcnt lgkmcnt(8)
	v_mfma_f32_16x16x32_f16 v[24:27], v[32:35], v[20:23], v[24:27]
	v_alignbit_b32 v11, v10, v11, 16
	v_alignbit_b32 v7, v7, v10, 16
	v_lshlrev_b32_e32 v6, 4, v6
	v_mfma_f32_16x16x32_f16 v[28:31], v[40:43], v[20:23], v[28:31]
	v_lshlrev_b32_e32 v8, 4, v8
	s_movk_i32 s4, 0xc0
	v_and_b32_e32 v10, 15, v0
	v_mfma_f32_16x16x32_f16 v[32:35], v[52:55], v[20:23], v[36:39]
	v_cmp_gt_u32_e32 vcc, 10, v10
	v_mfma_f32_16x16x32_f16 v[36:39], v[60:63], v[20:23], v[44:47]
	v_mfma_f32_16x16x32_f16 v[40:43], v[68:71], v[20:23], v[48:51]
	s_nop 2
	global_load_dwordx4 v[48:51], v106, s[6:7] offset:16
	global_load_dwordx4 v[52:55], v106, s[6:7]
	ds_read_b128 v[60:63], v104 offset:2048
	v_mfma_f32_16x16x32_f16 v[56:59], v[56:59], v[2:5], 0
	v_mfma_f32_16x16x32_f16 v[64:67], v[64:67], v[2:5], 0
	s_waitcnt lgkmcnt(8)
	v_mfma_f32_16x16x32_f16 v[2:5], v[72:75], v[2:5], 0
	s_waitcnt lgkmcnt(7)
	v_mfma_f32_16x16x32_f16 v[44:47], v[76:79], v[20:23], v[56:59]
	s_waitcnt lgkmcnt(6)
	v_mfma_f32_16x16x32_f16 v[56:59], v[80:83], v[20:23], v[64:67]
	s_waitcnt lgkmcnt(5)
	v_mfma_f32_16x16x32_f16 v[2:5], v[84:87], v[20:23], v[2:5]
	ds_read_b128 v[18:21], v104 offset:6144
	ds_read_b128 v[64:67], v104 offset:10240
	ds_read_b128 v[68:71], v104 offset:3072
	s_waitcnt lgkmcnt(3)
	v_mfma_f32_16x16x32_f16 v[22:25], v[60:63], v[14:17], v[24:27]
	ds_read_b128 v[60:63], v104 offset:14336
	ds_read_b128 v[72:75], v104 offset:7168
	s_waitcnt lgkmcnt(4)
	v_mfma_f32_16x16x32_f16 v[18:21], v[18:21], v[14:17], v[28:31]
	s_nop 2
	ds_read_b128 v[26:29], v104 offset:18432
	ds_read_b128 v[76:79], v104 offset:22528
	ds_read_b128 v[80:83], v104 offset:11264
	s_waitcnt lgkmcnt(6)
	v_mfma_f32_16x16x32_f16 v[30:33], v[64:67], v[14:17], v[32:35]
	ds_read_b128 v[64:67], v104 offset:15360
	global_load_dwordx4 v[84:87], v106, s[6:7] offset:144
	global_load_dwordx4 v[88:91], v106, s[6:7] offset:128
	s_waitcnt lgkmcnt(3)
	v_mfma_f32_16x16x32_f16 v[26:29], v[26:29], v[14:17], v[40:43]
	s_waitcnt lgkmcnt(2)
	v_mfma_f32_16x16x32_f16 v[42:45], v[76:79], v[14:17], v[44:47]
	ds_bpermute_b32 v76, v105, v13
	ds_bpermute_b32 v77, v105, v12
	ds_bpermute_b32 v78, v105, v11
	ds_bpermute_b32 v79, v105, v7
	v_mfma_f32_16x16x32_f16 v[34:37], v[60:63], v[14:17], v[36:39]
	ds_read_b128 v[60:63], v104 offset:26624
	ds_read_b128 v[92:95], v104 offset:19456
	s_nop 0
	ds_read_b128 v[38:41], v104 offset:30720
	ds_read_b128 v[96:99], v104 offset:23552
	ds_read_b128 v[100:103], v104 offset:27648
	s_waitcnt lgkmcnt(4)
	v_mfma_f32_16x16x32_f16 v[56:59], v[60:63], v[14:17], v[56:59]
	ds_read_b128 v[60:63], v104 offset:31744
	v_mov_b32_e32 v7, 0
	s_waitcnt lgkmcnt(3)
	v_mfma_f32_16x16x32_f16 v[2:5], v[38:41], v[14:17], v[2:5]
	global_load_dwordx4 v[38:41], v106, s[6:7] offset:272
	v_mfma_f32_16x16x32_f16 v[12:15], v[68:71], v[76:79], v[22:25]
	s_nop 2
	global_load_dwordx4 v[22:25], v106, s[6:7] offset:256
	v_mfma_f32_16x16x32_f16 v[34:37], v[64:67], v[76:79], v[34:37]
	global_load_dwordx4 v[64:67], v106, s[6:7] offset:400
	global_load_dwordx4 v[68:71], v106, s[6:7] offset:384
	s_waitcnt vmcnt(6)
	v_pk_add_f32 v[12:13], v[12:13], v[52:53]
	v_mfma_f32_16x16x32_f16 v[16:19], v[72:75], v[76:79], v[18:21]
	v_lshl_add_u64 v[72:73], s[10:11], 0, v[6:7]
	v_lshlrev_b32_e32 v6, 1, v9
	v_pk_add_f32 v[14:15], v[14:15], v[54:55]
	v_lshl_add_u64 v[20:21], s[8:9], 0, v[6:7]
	v_lshlrev_b32_e32 v6, 6, v0
	v_and_b32_e32 v9, 60, v0
	v_cvt_pk_f16_f32 v12, v12, v13
	v_cvt_pk_f16_f32 v13, v14, v15
	v_pk_add_f32 v[14:15], v[16:17], v[48:49]
	v_pk_add_f32 v[16:17], v[18:19], v[50:51]
	v_or_b32_e32 v54, v8, v1
	v_and_or_b32 v6, v6, s4, v9
	v_cvt_pk_f16_f32 v14, v14, v15
	v_cvt_pk_f16_f32 v15, v16, v17
	v_ashrrev_i32_e32 v55, 31, v54
	ds_bpermute_b32 v16, v6, v12
	ds_bpermute_b32 v17, v6, v13
	ds_bpermute_b32 v18, v6, v14
	ds_bpermute_b32 v19, v6, v15
	v_lshlrev_b64 v[46:47], 8, v[54:55]
	v_mfma_f32_16x16x32_f16 v[30:33], v[80:83], v[76:79], v[30:33]
	v_lshl_add_u64 v[74:75], v[20:21], 0, v[46:47]
	global_load_dwordx4 v[46:49], v104, s[12:13]
	global_load_dwordx4 v[50:53], v104, s[12:13] offset:1024
	v_mfma_f32_16x16x32_f16 v[26:29], v[92:95], v[76:79], v[26:29]
	s_waitcnt lgkmcnt(0)
	global_store_dwordx4 v[74:75], v[16:19], off
	v_cvt_f32_f16_e32 v9, v16
	v_cvt_f32_f16_sdwa v11, v16 dst_sel:DWORD dst_unused:UNUSED_PAD src0_sel:WORD_1
	v_mfma_f32_16x16x32_f16 v[42:45], v[96:99], v[76:79], v[42:45]
	v_cvt_f32_f16_e32 v80, v19
	v_cvt_f32_f16_sdwa v81, v19 dst_sel:DWORD dst_unused:UNUSED_PAD src0_sel:WORD_1
	s_waitcnt vmcnt(5)
	v_pk_add_f32 v[20:21], v[26:27], v[22:23]
	v_mfma_f32_16x16x32_f16 v[56:59], v[100:103], v[76:79], v[56:59]
	v_add_f32_e64 v22, v28, v24
	v_add_f32_e64 v23, v29, v25
	v_cvt_pk_f16_f32 v20, v20, v21
	v_cvt_pk_f16_f32 v21, v22, v23
	v_mfma_f32_16x16x32_f16 v[2:5], v[60:63], v[76:79], v[2:5]
	v_cvt_f32_f16_e32 v76, v17
	v_cvt_f32_f16_sdwa v77, v17 dst_sel:DWORD dst_unused:UNUSED_PAD src0_sel:WORD_1
	v_pk_add_f32 v[16:17], v[30:31], v[88:89]
	v_cvt_f32_f16_e32 v78, v18
	v_cvt_pk_f16_f32 v30, v16, v17
	v_pk_add_f32 v[16:17], v[32:33], v[90:91]
	v_cvt_f32_f16_sdwa v79, v18 dst_sel:DWORD dst_unused:UNUSED_PAD src0_sel:WORD_1
	v_cvt_pk_f16_f32 v31, v16, v17
	v_pk_add_f32 v[16:17], v[34:35], v[84:85]
	global_load_dwordx4 v[60:63], v104, s[12:13] offset:3072
	v_cvt_pk_f16_f32 v32, v16, v17
	v_pk_add_f32 v[16:17], v[36:37], v[86:87]
	v_pk_add_f32 v[22:23], v[42:43], v[38:39]
	v_cvt_pk_f16_f32 v33, v16, v17
	global_load_dwordx4 v[16:19], v104, s[12:13] offset:2048
	v_pk_add_f32 v[24:25], v[44:45], v[40:41]
	v_cvt_pk_f16_f32 v22, v22, v23
	v_cvt_pk_f16_f32 v23, v24, v25
	ds_bpermute_b32 v24, v6, v20
	ds_bpermute_b32 v25, v6, v21
	ds_bpermute_b32 v26, v6, v22
	ds_bpermute_b32 v27, v6, v23
	ds_bpermute_b32 v34, v6, v30
	ds_bpermute_b32 v35, v6, v31
	ds_bpermute_b32 v36, v6, v32
	ds_bpermute_b32 v37, v6, v33
	s_waitcnt lgkmcnt(4)
	global_store_dwordx4 v[74:75], v[24:27], off offset:128
	v_cvt_f32_f16_e32 v40, v24
	v_cvt_f32_f16_sdwa v41, v24 dst_sel:DWORD dst_unused:UNUSED_PAD src0_sel:WORD_1
	v_cvt_f32_f16_e32 v42, v25
	v_cvt_f32_f16_sdwa v43, v25 dst_sel:DWORD dst_unused:UNUSED_PAD src0_sel:WORD_1
	s_waitcnt vmcnt(6)
	v_pk_add_f32 v[24:25], v[56:57], v[68:69]
	v_pk_add_f32 v[2:3], v[2:3], v[64:65]
	s_waitcnt lgkmcnt(0)
	global_store_dwordx4 v[74:75], v[34:37], off offset:64
	v_cvt_f32_f16_e32 v82, v34
	v_cvt_f32_f16_sdwa v83, v34 dst_sel:DWORD dst_unused:UNUSED_PAD src0_sel:WORD_1
	v_cvt_f32_f16_e32 v28, v36
	v_cvt_f32_f16_sdwa v29, v36 dst_sel:DWORD dst_unused:UNUSED_PAD src0_sel:WORD_1
	v_cvt_pk_f16_f32 v34, v24, v25
	v_pk_add_f32 v[24:25], v[58:59], v[70:71]
	v_cvt_pk_f16_f32 v36, v2, v3
	v_pk_add_f32 v[2:3], v[4:5], v[66:67]
	v_cvt_f32_f16_e32 v84, v35
	v_cvt_f32_f16_sdwa v85, v35 dst_sel:DWORD dst_unused:UNUSED_PAD src0_sel:WORD_1
	v_cvt_f32_f16_e32 v38, v37
	v_cvt_f32_f16_sdwa v39, v37 dst_sel:DWORD dst_unused:UNUSED_PAD src0_sel:WORD_1
	v_cvt_pk_f16_f32 v35, v24, v25
	v_cvt_pk_f16_f32 v37, v2, v3
	ds_bpermute_b32 v2, v6, v34
	ds_bpermute_b32 v3, v6, v35
	ds_bpermute_b32 v4, v6, v36
	ds_bpermute_b32 v5, v6, v37
	v_cvt_f32_f16_e32 v6, v26
	v_cvt_f32_f16_sdwa v26, v26 dst_sel:DWORD dst_unused:UNUSED_PAD src0_sel:WORD_1
	v_cvt_f32_f16_e32 v44, v27
	v_cvt_f32_f16_sdwa v45, v27 dst_sel:DWORD dst_unused:UNUSED_PAD src0_sel:WORD_1
	s_waitcnt lgkmcnt(0)
	global_store_dwordx4 v[74:75], v[2:5], off offset:192
	v_cvt_f32_f16_e32 v27, v2
	v_cvt_f32_f16_sdwa v56, v2 dst_sel:DWORD dst_unused:UNUSED_PAD src0_sel:WORD_1
	v_mov_b32_e32 v2, v7
	s_waitcnt vmcnt(7)
	v_mfma_f32_16x16x32_f16 v[12:15], v[12:15], v[46:49], 0
	v_cvt_f32_f16_e32 v59, v4
	v_cvt_pk_fp8_f32 v2, v9, v11
	v_cvt_f32_f16_sdwa v9, v4 dst_sel:DWORD dst_unused:UNUSED_PAD src0_sel:WORD_1
	v_mov_b32_e32 v25, v7
	v_cvt_f32_f16_e32 v57, v3
	v_cvt_f32_f16_sdwa v58, v3 dst_sel:DWORD dst_unused:UNUSED_PAD src0_sel:WORD_1
	v_cvt_f32_f16_e32 v11, v5
	v_cvt_f32_f16_sdwa v64, v5 dst_sel:DWORD dst_unused:UNUSED_PAD src0_sel:WORD_1
	v_mov_b32_e32 v3, v7
	v_mov_b32_e32 v4, v7
	v_mov_b32_e32 v5, v7
	v_cvt_pk_fp8_f32 v25, v6, v26
	v_mov_b32_e32 v26, v7
	v_cvt_pk_fp8_f32 v3, v78, v79
	v_cvt_pk_fp8_f32 v4, v82, v83
	v_cvt_pk_fp8_f32 v5, v28, v29
	v_mov_b32_e32 v24, v7
	v_cvt_pk_fp8_f32 v26, v27, v56
	v_mov_b32_e32 v27, v7
	s_waitcnt vmcnt(6)
	v_mfma_f32_16x16x32_f16 v[12:15], v[30:33], v[50:53], v[12:15]
	v_cvt_pk_fp8_f32 v24, v40, v41
	v_cvt_pk_fp8_f32 v27, v59, v9
	v_cvt_pk_fp8_f32 v2, v76, v77 op_sel:[0,0,1]
	v_cvt_pk_fp8_f32 v3, v80, v81 op_sel:[0,0,1]
	v_cvt_pk_fp8_f32 v4, v84, v85 op_sel:[0,0,1]
	v_cvt_pk_fp8_f32 v5, v38, v39 op_sel:[0,0,1]
	s_waitcnt vmcnt(3)
	v_mfma_f32_16x16x32_f16 v[12:15], v[20:23], v[16:19], v[12:15]
	v_cvt_pk_fp8_f32 v24, v42, v43 op_sel:[0,0,1]
	v_cvt_pk_fp8_f32 v25, v44, v45 op_sel:[0,0,1]
	v_cvt_pk_fp8_f32 v26, v57, v58 op_sel:[0,0,1]
	v_cvt_pk_fp8_f32 v27, v11, v64 op_sel:[0,0,1]
	v_lshlrev_b64 v[28:29], 7, v[54:55]
	v_lshl_add_u64 v[16:17], v[72:73], 0, v[28:29]
	global_store_dwordx4 v[16:17], v[2:5], off
	global_store_dwordx4 v[16:17], v[24:27], off offset:64
	s_nop 0
	v_mfma_f32_16x16x32_f16 v[2:5], v[34:37], v[60:63], v[12:15]
	s_and_b64 exec, exec, vcc
	s_cbranch_execz .LBB1_8
	v_lshlrev_b32_e32 v6, 4, v10
	v_lshlrev_b32_e32 v6, 1, v6
	v_and_b32_e32 v1, 12, v1
	v_lshl_add_u64 v[10:11], s[14:15], 0, v[6:7]
	v_lshlrev_b32_e32 v6, 1, v1
	v_lshl_add_u64 v[6:7], v[10:11], 0, v[6:7]
	v_mul_u32_u24_e32 v8, 10, v8
	v_ashrrev_i32_e32 v9, 31, v8
	v_lshl_add_u64 v[6:7], v[8:9], 1, v[6:7]
	v_cvt_pk_f16_f32 v5, v4, v5
	v_cvt_pk_f16_f32 v4, v2, v3
	global_store_dwordx2 v[6:7], v[4:5], off

.LBB4_10:
	s_or_b64 exec, exec, s[4:5]
	s_waitcnt vmcnt(0)
	s_waitcnt lgkmcnt(0)
	s_barrier
	s_cmp_ge_u32 s23, 0x1000
	s_cbranch_scc0 .Lmlp_noprio
	s_setprio 1
.Lmlp_noprio:
	s_and_saveexec_b64 s[0:1], vcc
	s_cbranch_execz .LBB4_12
	v_lshlrev_b32_e32 v19, 5, v23
	ds_read_b128 v[24:27], v19 offset:40960
	ds_read_b128 v[28:31], v19 offset:40976
	ds_read_b128 v[32:35], v19 offset:41472
	v_lshrrev_b32_e32 v64, 4, v22
	v_and_or_b32 v18, v18, 60, v64
	v_lshlrev_b32_e32 v18, 2, v18
	v_lshlrev_b32_e32 v65, 4, v22
	s_waitcnt lgkmcnt(0)
	v_fma_mix_f32 v20, v24, v14, v32 op_sel_hi:[0,1,0]
	v_fma_mix_f32 v14, v25, v14, v33 op_sel:[0,1,0] op_sel_hi:[0,1,0]
	v_fma_mix_f32 v21, v26, v15, v34 op_sel_hi:[0,1,0]
	v_fma_mix_f32 v15, v27, v15, v35 op_sel:[0,1,0] op_sel_hi:[0,1,0]
	ds_read_b128 v[24:27], v19 offset:41488
	v_max_f32_e32 v20, 0, v20
	v_max_f32_e32 v14, 0, v14
	v_max_f32_e32 v21, 0, v21
	v_max_f32_e32 v15, 0, v15
	s_waitcnt lgkmcnt(0)
	v_fma_mix_f32 v23, v28, v16, v24 op_sel_hi:[0,1,0]
	v_fma_mix_f32 v24, v30, v17, v26 op_sel_hi:[0,1,0]
	v_fma_mix_f32 v17, v31, v17, v27 op_sel:[0,1,0] op_sel_hi:[0,1,0]
	v_max_f32_e32 v24, 0, v24
	v_max_f32_e32 v17, 0, v17
	v_fma_mix_f32 v16, v29, v16, v25 op_sel:[0,1,0] op_sel_hi:[0,1,0]
	v_cvt_pk_f16_f32 v17, v24, v17
	ds_read_b128 v[24:27], v19 offset:41088
	ds_read_b128 v[28:31], v19 offset:41600
	v_cvt_pk_f16_f32 v15, v21, v15
	v_cvt_pk_f16_f32 v14, v20, v14
	v_max_f32_e32 v23, 0, v23
	v_max_f32_e32 v16, 0, v16
	s_waitcnt lgkmcnt(0)
	v_fma_mix_f32 v20, v24, v6, v28 op_sel_hi:[0,1,0]
	v_fma_mix_f32 v6, v25, v6, v29 op_sel:[0,1,0] op_sel_hi:[0,1,0]
	v_fma_mix_f32 v21, v26, v7, v30 op_sel_hi:[0,1,0]
	v_fma_mix_f32 v7, v27, v7, v31 op_sel:[0,1,0] op_sel_hi:[0,1,0]
	ds_read_b128 v[24:27], v19 offset:41104
	ds_read_b128 v[28:31], v19 offset:41616
	v_cvt_pk_f16_f32 v16, v23, v16
	v_max_f32_e32 v20, 0, v20
	v_max_f32_e32 v6, 0, v6
	v_max_f32_e32 v21, 0, v21
	s_waitcnt lgkmcnt(0)
	v_fma_mix_f32 v23, v24, v8, v28 op_sel_hi:[0,1,0]
	v_fma_mix_f32 v24, v26, v9, v30 op_sel_hi:[0,1,0]
	v_fma_mix_f32 v9, v27, v9, v31 op_sel:[0,1,0] op_sel_hi:[0,1,0]
	v_max_f32_e32 v24, 0, v24
	v_max_f32_e32 v9, 0, v9
	v_fma_mix_f32 v8, v25, v8, v29 op_sel:[0,1,0] op_sel_hi:[0,1,0]
	v_cvt_pk_f16_f32 v9, v24, v9
	ds_read_b128 v[24:27], v19 offset:41216
	ds_read_b128 v[28:31], v19 offset:41728
	v_max_f32_e32 v7, 0, v7
	v_cvt_pk_f16_f32 v7, v21, v7
	v_cvt_pk_f16_f32 v6, v20, v6
	v_max_f32_e32 v23, 0, v23
	s_waitcnt lgkmcnt(0)
	v_fma_mix_f32 v20, v24, v10, v28 op_sel_hi:[0,1,0]
	v_fma_mix_f32 v10, v25, v10, v29 op_sel:[0,1,0] op_sel_hi:[0,1,0]
	v_fma_mix_f32 v21, v26, v11, v30 op_sel_hi:[0,1,0]
	v_fma_mix_f32 v11, v27, v11, v31 op_sel:[0,1,0] op_sel_hi:[0,1,0]
	ds_read_b128 v[24:27], v19 offset:41232
	ds_read_b128 v[28:31], v19 offset:41744
	v_max_f32_e32 v8, 0, v8
	v_cvt_pk_f16_f32 v8, v23, v8
	v_max_f32_e32 v20, 0, v20
	v_max_f32_e32 v10, 0, v10
	s_waitcnt lgkmcnt(0)
	v_fma_mix_f32 v23, v24, v12, v28 op_sel_hi:[0,1,0]
	v_fma_mix_f32 v24, v26, v13, v30 op_sel_hi:[0,1,0]
	v_fma_mix_f32 v13, v27, v13, v31 op_sel:[0,1,0] op_sel_hi:[0,1,0]
	v_max_f32_e32 v24, 0, v24
	v_max_f32_e32 v13, 0, v13
	v_fma_mix_f32 v12, v25, v12, v29 op_sel:[0,1,0] op_sel_hi:[0,1,0]
	v_cvt_pk_f16_f32 v13, v24, v13
	ds_read_b128 v[24:27], v19 offset:41344
	ds_read_b128 v[28:31], v19 offset:41856
	v_max_f32_e32 v21, 0, v21
	v_max_f32_e32 v11, 0, v11
	v_cvt_pk_f16_f32 v11, v21, v11
	v_cvt_pk_f16_f32 v10, v20, v10
	s_waitcnt lgkmcnt(0)
	v_fma_mix_f32 v20, v24, v2, v28 op_sel_hi:[0,1,0]
	v_fma_mix_f32 v2, v25, v2, v29 op_sel:[0,1,0] op_sel_hi:[0,1,0]
	v_fma_mix_f32 v21, v26, v3, v30 op_sel_hi:[0,1,0]
	v_fma_mix_f32 v3, v27, v3, v31 op_sel:[0,1,0] op_sel_hi:[0,1,0]
	ds_read_b128 v[24:27], v19 offset:41360
	ds_read_b128 v[28:31], v19 offset:41872
	ds_bpermute_b32 v14, v18, v14
	ds_bpermute_b32 v15, v18, v15
	ds_bpermute_b32 v16, v18, v16
	ds_bpermute_b32 v17, v18, v17
	v_max_f32_e32 v23, 0, v23
	v_max_f32_e32 v12, 0, v12
	v_cvt_pk_f16_f32 v12, v23, v12
	s_waitcnt lgkmcnt(4)
	v_fma_mix_f32 v19, v24, v4, v28 op_sel_hi:[0,1,0]
	v_fma_mix_f32 v4, v25, v4, v29 op_sel:[0,1,0] op_sel_hi:[0,1,0]
	v_fma_mix_f32 v23, v26, v5, v30 op_sel_hi:[0,1,0]
	v_fma_mix_f32 v5, v27, v5, v31 op_sel:[0,1,0] op_sel_hi:[0,1,0]
	v_max_f32_e32 v20, 0, v20
	v_max_f32_e32 v2, 0, v2
	v_max_f32_e32 v21, 0, v21
	v_max_f32_e32 v3, 0, v3
	v_max_f32_e32 v19, 0, v19
	v_max_f32_e32 v4, 0, v4
	v_max_f32_e32 v23, 0, v23
	v_max_f32_e32 v5, 0, v5
	v_cvt_pk_f16_f32 v5, v23, v5
	v_cvt_pk_f16_f32 v4, v19, v4
	v_cvt_pk_f16_f32 v3, v21, v3
	v_cvt_pk_f16_f32 v2, v20, v2
	ds_bpermute_b32 v6, v18, v6
	ds_bpermute_b32 v7, v18, v7
	ds_bpermute_b32 v8, v18, v8
	ds_bpermute_b32 v9, v18, v9
	ds_bpermute_b32 v10, v18, v10
	ds_bpermute_b32 v11, v18, v11
	ds_bpermute_b32 v12, v18, v12
	ds_bpermute_b32 v13, v18, v13
	ds_bpermute_b32 v2, v18, v2
	ds_bpermute_b32 v3, v18, v3
	ds_bpermute_b32 v4, v18, v4
	ds_bpermute_b32 v5, v18, v5
	ds_read_b128 v[18:21], v65
	ds_read_b128 v[22:25], v65 offset:4096
	ds_read_b128 v[26:29], v65 offset:8192
	ds_read_b128 v[42:45], v65 offset:12288
	s_waitcnt lgkmcnt(3)
	v_mfma_f32_16x16x32_f16 v[30:33], v[14:17], v[18:21], 0
	s_waitcnt lgkmcnt(2)
	v_mfma_f32_16x16x32_f16 v[34:37], v[14:17], v[22:25], 0
	ds_read_b128 v[18:21], v65 offset:16384
	ds_read_b128 v[22:25], v65 offset:20480
	ds_read_b128 v[46:49], v65 offset:24576
	ds_read_b128 v[50:53], v65 offset:28672
	s_waitcnt lgkmcnt(5)
	v_mfma_f32_16x16x32_f16 v[38:41], v[14:17], v[26:29], 0
	s_waitcnt lgkmcnt(4)
	v_mfma_f32_16x16x32_f16 v[42:45], v[14:17], v[42:45], 0
	s_waitcnt lgkmcnt(3)
	v_mfma_f32_16x16x32_f16 v[26:29], v[14:17], v[18:21], 0
	s_waitcnt lgkmcnt(2)
	v_mfma_f32_16x16x32_f16 v[22:25], v[14:17], v[22:25], 0
	s_waitcnt lgkmcnt(1)
	v_mfma_f32_16x16x32_f16 v[18:21], v[14:17], v[46:49], 0
	s_waitcnt lgkmcnt(0)
	v_mfma_f32_16x16x32_f16 v[14:17], v[14:17], v[50:53], 0
	ds_read_b128 v[46:49], v65 offset:1024
	ds_read_b128 v[50:53], v65 offset:5120
	ds_read_b128 v[54:57], v65 offset:9216
	ds_read_b128 v[58:61], v65 offset:13312
	s_waitcnt lgkmcnt(3)
	v_mfma_f32_16x16x32_f16 v[30:33], v[6:9], v[46:49], v[30:33]
	s_waitcnt lgkmcnt(2)
	v_mfma_f32_16x16x32_f16 v[34:37], v[6:9], v[50:53], v[34:37]
	s_waitcnt lgkmcnt(1)
	v_mfma_f32_16x16x32_f16 v[38:41], v[6:9], v[54:57], v[38:41]
	s_waitcnt lgkmcnt(0)
	v_mfma_f32_16x16x32_f16 v[42:45], v[6:9], v[58:61], v[42:45]
	ds_read_b128 v[58:61], v65 offset:17408
	ds_read_b128 v[54:57], v65 offset:21504
	ds_read_b128 v[50:53], v65 offset:25600
	ds_read_b128 v[46:49], v65 offset:29696
	s_waitcnt lgkmcnt(3)
	v_mfma_f32_16x16x32_f16 v[26:29], v[6:9], v[58:61], v[26:29]
	s_waitcnt lgkmcnt(2)
	v_mfma_f32_16x16x32_f16 v[22:25], v[6:9], v[54:57], v[22:25]
	s_waitcnt lgkmcnt(1)
	v_mfma_f32_16x16x32_f16 v[18:21], v[6:9], v[50:53], v[18:21]
	s_waitcnt lgkmcnt(0)
	v_mfma_f32_16x16x32_f16 v[14:17], v[6:9], v[46:49], v[14:17]
	ds_read_b128 v[6:9], v65 offset:2048
	ds_read_b128 v[46:49], v65 offset:6144
	ds_read_b128 v[50:53], v65 offset:10240
	ds_read_b128 v[54:57], v65 offset:14336
	s_waitcnt lgkmcnt(3)
	v_mfma_f32_16x16x32_f16 v[30:33], v[10:13], v[6:9], v[30:33]
	s_waitcnt lgkmcnt(2)
	v_mfma_f32_16x16x32_f16 v[46:49], v[10:13], v[46:49], v[34:37]
	s_waitcnt lgkmcnt(1)
	v_mfma_f32_16x16x32_f16 v[50:53], v[10:13], v[50:53], v[38:41]
	s_waitcnt lgkmcnt(0)
	v_mfma_f32_16x16x32_f16 v[42:45], v[10:13], v[54:57], v[42:45]
	ds_read_b128 v[6:9], v65 offset:18432
	ds_read_b128 v[34:37], v65 offset:22528
	ds_read_b128 v[38:41], v65 offset:26624
	ds_read_b128 v[54:57], v65 offset:30720
	s_waitcnt lgkmcnt(3)
	v_mfma_f32_16x16x32_f16 v[6:9], v[10:13], v[6:9], v[26:29]
	s_waitcnt lgkmcnt(2)
	v_mfma_f32_16x16x32_f16 v[26:29], v[10:13], v[34:37], v[22:25]
	s_waitcnt lgkmcnt(1)
	v_mfma_f32_16x16x32_f16 v[34:37], v[10:13], v[38:41], v[18:21]
	s_waitcnt lgkmcnt(0)
	v_mfma_f32_16x16x32_f16 v[38:41], v[10:13], v[54:57], v[14:17]
	ds_read_b128 v[10:13], v65 offset:3072
	s_nop 1
	ds_read_b128 v[14:17], v65 offset:7168
	ds_read_b128 v[54:57], v65 offset:11264
	ds_read_b128 v[58:61], v65 offset:15360
	s_waitcnt lgkmcnt(3)
	v_mfma_f32_16x16x32_f16 v[22:25], v[2:5], v[10:13], v[30:33]
	s_waitcnt lgkmcnt(2)
	v_mfma_f32_16x16x32_f16 v[18:21], v[2:5], v[14:17], v[46:49]
	s_waitcnt lgkmcnt(1)
	v_mfma_f32_16x16x32_f16 v[14:17], v[2:5], v[54:57], v[50:53]
	s_waitcnt lgkmcnt(0)
	v_mfma_f32_16x16x32_f16 v[10:13], v[2:5], v[58:61], v[42:45]
	ds_read_b128 v[30:33], v65 offset:19456
	s_nop 1
	ds_read_b128 v[42:45], v65 offset:23552
	ds_read_b128 v[46:49], v65 offset:27648
	ds_read_b128 v[50:53], v65 offset:31744
	v_lshlrev_b32_e32 v59, 2, v64
	v_lshlrev_b32_e32 v58, 10, v62
	s_waitcnt lgkmcnt(3)
	v_mfma_f32_16x16x32_f16 v[30:33], v[2:5], v[30:33], v[6:9]
	s_waitcnt lgkmcnt(1)
	v_mfma_f32_16x16x32_f16 v[6:9], v[2:5], v[46:49], v[34:37]
	s_nop 2
	v_lshlrev_b32_e32 v34, 3, v0
	v_mfma_f32_16x16x32_f16 v[26:29], v[2:5], v[42:45], v[26:29]
	v_and_b32_e32 v44, 0x78, v34
	v_lshlrev_b32_e32 v34, 4, v63
	v_ashrrev_i32_e32 v35, 31, v34
	v_lshl_add_u64 v[36:37], v[34:35], 2, s[8:9]
	v_and_b32_e32 v42, 48, v0
	v_mov_b32_e32 v43, 0
	v_lshl_add_u64 v[36:37], v[36:37], 0, v[42:43]
	v_lshlrev_b32_e32 v42, 1, v44
	v_lshlrev_b32_e32 v60, 2, v44
	s_waitcnt lgkmcnt(0)
	v_mfma_f32_16x16x32_f16 v[2:5], v[2:5], v[50:53], v[38:41]
	v_or_b32_e32 v48, v34, v59
	v_lshl_add_u64 v[46:47], s[12:13], 0, v[42:43]
	v_mov_b32_e32 v52, v14
	global_load_dwordx4 v[38:41], v[36:37], off
	s_nop 0
	global_load_dwordx4 v[34:37], v60, s[6:7] offset:16
	global_load_dwordx4 v[42:45], v60, s[6:7]
	v_mov_b32_e32 v53, v10
	v_mov_b32_e32 v50, v22
	v_mov_b32_e32 v51, v18
	v_ashrrev_i32_e32 v49, 31, v48
	v_mov_b32_e32 v18, v23
	v_mov_b32_e32 v10, v15
	v_lshlrev_b64 v[66:67], 8, v[48:49]
	v_lshl_add_u64 v[66:67], v[46:47], 0, v[66:67]
	s_waitcnt vmcnt(0)
	v_pk_add_f32 v[52:53], v[44:45], v[52:53]
	s_nop 0
	v_pk_mul_f32 v[54:55], v[38:39], v[52:53] op_sel_hi:[0,1]
	v_mov_b32_e32 v52, v30
	v_mov_b32_e32 v53, v26
	v_pk_add_f32 v[52:53], v[34:35], v[52:53]
	v_pk_add_f32 v[50:51], v[42:43], v[50:51]
	v_pk_mul_f32 v[56:57], v[38:39], v[52:53] op_sel_hi:[0,1]
	v_mov_b32_e32 v52, v6
	v_mov_b32_e32 v53, v2
	v_pk_add_f32 v[52:53], v[36:37], v[52:53]
	v_mov_b32_e32 v26, v31
	v_mov_b32_e32 v2, v7
	v_or_b32_e32 v6, 1, v48
	v_pk_mul_f32 v[50:51], v[38:39], v[50:51] op_sel_hi:[0,1]
	v_pk_mul_f32 v[52:53], v[38:39], v[52:53] op_sel_hi:[0,1]
	v_pk_add_f32 v[18:19], v[42:43], v[18:19]
	v_pk_add_f32 v[10:11], v[44:45], v[10:11]
	v_pk_add_f32 v[14:15], v[34:35], v[26:27]
	v_pk_add_f32 v[2:3], v[36:37], v[2:3]
	v_ashrrev_i32_e32 v7, 31, v6
	v_cvt_pk_f16_f32 v62, v50, v51
	v_cvt_pk_f16_f32 v63, v54, v55
	v_cvt_pk_f16_f32 v64, v56, v57
	v_cvt_pk_f16_f32 v65, v52, v53
	v_pk_mul_f32 v[18:19], v[38:39], v[18:19] op_sel:[1,0]
	v_pk_mul_f32 v[10:11], v[38:39], v[10:11] op_sel:[1,0]
	v_pk_mul_f32 v[22:23], v[38:39], v[14:15] op_sel:[1,0]
	v_pk_mul_f32 v[2:3], v[38:39], v[2:3] op_sel:[1,0]
	v_lshlrev_b64 v[6:7], 8, v[6:7]
	global_store_dwordx4 v[66:67], v[62:65], off sc0 sc1
	v_lshl_add_u64 v[6:7], v[46:47], 0, v[6:7]
	s_nop 0
	v_cvt_pk_f16_f32 v62, v18, v19
	v_cvt_pk_f16_f32 v63, v10, v11
	v_cvt_pk_f16_f32 v64, v22, v23
	v_cvt_pk_f16_f32 v65, v2, v3
	global_store_dwordx4 v[6:7], v[62:65], off sc0 sc1
	v_mov_b32_e32 v6, v24
	v_mov_b32_e32 v7, v20
	v_pk_add_f32 v[6:7], v[42:43], v[6:7]
	v_mov_b32_e32 v20, v25
	v_pk_mul_f32 v[14:15], v[40:41], v[6:7] op_sel_hi:[0,1]
	v_mov_b32_e32 v6, v16
	v_mov_b32_e32 v7, v12
	v_pk_add_f32 v[6:7], v[44:45], v[6:7]
	v_mov_b32_e32 v12, v17
	v_pk_mul_f32 v[30:31], v[40:41], v[6:7] op_sel_hi:[0,1]
	v_mov_b32_e32 v6, v32
	v_mov_b32_e32 v7, v28
	v_pk_add_f32 v[6:7], v[34:35], v[6:7]
	v_mov_b32_e32 v16, v41
	v_pk_mul_f32 v[38:39], v[40:41], v[6:7] op_sel_hi:[0,1]
	v_mov_b32_e32 v6, v8
	v_mov_b32_e32 v7, v4
	v_pk_add_f32 v[6:7], v[36:37], v[6:7]
	v_pk_add_f32 v[12:13], v[44:45], v[12:13]
	v_pk_mul_f32 v[26:27], v[40:41], v[6:7] op_sel_hi:[0,1]
	v_or_b32_e32 v6, 2, v48
	v_ashrrev_i32_e32 v7, 31, v6
	v_lshlrev_b64 v[6:7], 8, v[6:7]
	v_mov_b32_e32 v28, v33
	v_cvt_pk_f16_f32 v62, v14, v15
	v_cvt_pk_f16_f32 v63, v30, v31
	v_cvt_pk_f16_f32 v64, v38, v39
	v_cvt_pk_f16_f32 v65, v26, v27
	v_lshl_add_u64 v[6:7], v[46:47], 0, v[6:7]
	v_pk_mul_f32 v[24:25], v[16:17], v[12:13] op_sel_hi:[0,1]
	v_pk_add_f32 v[12:13], v[34:35], v[28:29]
	v_add_f32_e32 v4, 0, v52
	global_store_dwordx4 v[6:7], v[62:65], off sc0 sc1
	v_pk_add_f32 v[6:7], v[42:43], v[20:21]
	v_pk_mul_f32 v[28:29], v[16:17], v[12:13] op_sel_hi:[0,1]
	v_pk_mul_f32 v[12:13], v[2:3], v[2:3]
	v_add_f32_e32 v2, v2, v4
	v_pk_mul_f32 v[20:21], v[16:17], v[6:7] op_sel_hi:[0,1]
	v_add_f32_e32 v17, v26, v2
	v_add_f32_e32 v2, 0, v57
	v_add_f32_e32 v2, v23, v2
	v_pk_fma_f32 v[12:13], v[52:53], v[52:53], v[12:13]
	v_add_f32_e32 v2, v39, v2
	v_pk_fma_f32 v[32:33], v[26:27], v[26:27], v[12:13]
	v_pk_mul_f32 v[12:13], v[22:23], v[22:23]
	v_add_f32_e32 v26, v29, v2
	v_add_f32_e32 v2, 0, v56
	v_pk_fma_f32 v[12:13], v[56:57], v[56:57], v[12:13]
	v_add_f32_e32 v2, v22, v2
	v_pk_fma_f32 v[12:13], v[38:39], v[38:39], v[12:13]
	v_add_f32_e32 v2, v38, v2
	v_cvt_pk_f16_f32 v8, v28, v29
	v_pk_fma_f32 v[12:13], v[28:29], v[28:29], v[12:13]
	v_add_f32_e32 v28, v28, v2
	v_pk_mul_f32 v[22:23], v[10:11], v[10:11]
	v_add_f32_e32 v2, 0, v55
	v_pk_fma_f32 v[22:23], v[54:55], v[54:55], v[22:23]
	v_add_f32_e32 v2, v11, v2
	v_pk_fma_f32 v[22:23], v[30:31], v[30:31], v[22:23]
	v_add_f32_e32 v2, v31, v2
	v_cvt_pk_f16_f32 v7, v24, v25
	v_pk_fma_f32 v[22:23], v[24:25], v[24:25], v[22:23]
	v_add_f32_e32 v25, v25, v2
	v_add_f32_e32 v2, 0, v54
	v_add_f32_e32 v2, v10, v2
	v_add_f32_e32 v2, v30, v2
	v_add_f32_e32 v24, v24, v2
	v_add_f32_e32 v2, 0, v51
	v_pk_mul_f32 v[10:11], v[18:19], v[18:19]
	v_add_f32_e32 v2, v19, v2
	v_pk_fma_f32 v[10:11], v[50:51], v[50:51], v[10:11]
	v_add_f32_e32 v2, v15, v2
	v_pk_fma_f32 v[10:11], v[14:15], v[14:15], v[10:11]
	v_add_f32_e32 v15, v21, v2
	v_add_f32_e32 v2, 0, v50
	v_add_f32_e32 v2, v18, v2
	v_add_f32_e32 v2, v14, v2
	v_add_f32_e32 v14, v20, v2
	v_add_f32_e32 v2, 0, v53
	v_add_f32_e32 v2, v3, v2
	v_mov_b32_e32 v4, v9
	v_add_f32_e32 v18, v27, v2
	v_pk_add_f32 v[2:3], v[36:37], v[4:5]
	v_cvt_pk_f16_f32 v6, v20, v21
	v_pk_mul_f32 v[2:3], v[16:17], v[2:3] op_sel_hi:[0,1]
	v_cvt_pk_f16_f32 v9, v2, v3
	v_pk_fma_f32 v[4:5], v[2:3], v[2:3], v[32:33]
	v_add_f32_e32 v16, v2, v17
	v_or_b32_e32 v2, 3, v48
	v_add_f32_e32 v17, v3, v18
	v_ashrrev_i32_e32 v3, 31, v2
	v_lshlrev_b64 v[2:3], 8, v[2:3]
	v_lshl_add_u64 v[2:3], v[46:47], 0, v[2:3]
	v_permlane16_swap_b32_e32 v14, v15
	v_permlane16_swap_b32_e32 v24, v25
	global_store_dwordx4 v[2:3], v[6:9], off sc0 sc1
	v_add_f32_e32 v2, v14, v15
	v_add_f32_e32 v3, v24, v25
	v_permlane16_swap_b32_e32 v28, v26
	v_permlane16_swap_b32_e32 v16, v17
	v_permlane32_swap_b32_e32 v2, v3
	v_add_f32_e32 v6, v28, v26
	v_add_f32_e32 v7, v16, v17
	v_add_f32_e32 v2, v2, v3
	v_or3_b32 v3, v58, v60, v59
	v_permlane32_swap_b32_e32 v6, v7
	v_pk_fma_f32 v[10:11], v[20:21], v[20:21], v[10:11]
	v_add_f32_e32 v6, v6, v7
	v_add_u32_e32 v3, 0x8000, v3
	ds_write2_b32 v3, v2, v6 offset1:4
	v_mov_b32_e32 v2, v11
	v_mov_b32_e32 v6, v23
	s_nop 0
	v_permlane16_swap_b32_e32 v10, v2
	v_permlane16_swap_b32_e32 v22, v6
	v_add_f32_e32 v2, v10, v2
	v_add_f32_e32 v6, v22, v6
	s_nop 1
	v_permlane32_swap_b32_e32 v2, v6
	v_add_f32_e32 v2, v2, v6
	v_mov_b32_e32 v6, v13
	s_nop 1
	v_permlane16_swap_b32_e32 v12, v6
	v_permlane16_swap_b32_e32 v4, v5
	v_add_f32_e32 v6, v12, v6
	v_add_f32_e32 v4, v4, v5
	s_nop 1
	v_permlane32_swap_b32_e32 v6, v4
	v_add_f32_e32 v4, v6, v4
	ds_write2_b32 v3, v2, v4 offset0:128 offset1:132
